# FT warms its tile's k_final slot table in L2
# speedup vs baseline: 1.0104x; 1.0104x over previous
_Z6k_iterILb0ELb1EEvPKfS1_PKiPK15HIP_vector_typeIfLj4EES7_S1_S1_S3_S1_PfS8_S1_S3_PDF16_PS5_SA_PiSA_SB_:
	s_and_b32 s38, s0, 0xfffff000
	s_mov_b32 s39, s1
	s_load_dwordx2 s[8:9], s[0:1], 0x80
	s_load_dwordx4 s[4:7], s[0:1], 0x70
	s_load_dwordx4 s[16:19], s[0:1], 0x40
	s_load_dwordx2 s[22:23], s[0:1], 0x50
	s_load_dwordx2 s[42:43], s[0:1], 0x88
	v_readfirstlane_b32 s12, v0
	v_cmp_gt_u32_e64 s[14:15], 64, v0
	v_lshlrev_b32_e32 v1, 2, v0
	s_and_saveexec_b64 s[10:11], s[14:15]
	v_mov_b32_e32 v2, 0
	ds_write_b32 v1, v2 offset:5152
	s_or_b64 exec, exec, s[10:11]
	s_lshl_b32 s3, s2, 5
	s_and_b32 s3, s3, 0xe0
	s_lshr_b32 s2, s2, 3
	s_add_i32 s2, s3, s2
	s_lshl_b32 s29, s2, 6
	v_and_b32_e32 v2, 31, v0
	v_or_b32_e32 v4, s29, v2
	v_mov_b32_e32 v5, 0
	s_lshr_b32 s30, s12, 6
	s_lshl_b32 s32, s30, 2
	s_lshr_b32 s32, 0x73261540, s32
	s_lshl_b32 s32, s32, 5
	s_and_b32 s32, s32, 0xe0
	v_or_b32_e32 v176, s32, v2
	v_lshlrev_b32_e32 v177, 4, v176
	v_add_u32_e32 v178, 0x1000, v177
	v_add_u32_e32 v179, 0x2000, v177
	v_add_u32_e32 v180, 0x3000, v177
	v_add_u32_e32 v181, 0x4000, v177
	v_add_u32_e32 v182, 0x5000, v177
	s_mov_b32 s3, 0
	s_lshl_b64 s[34:35], s[2:3], 16
	s_lshl_b32 s33, s2, 2
	s_waitcnt lgkmcnt(0)
	s_load_dword s26, s[8:9], s33 offset:0x0
	s_add_u32 s20, s4, s34
	s_addc_u32 s21, s5, s35
	v_lshl_add_u64 v[4:5], v[4:5], 4, s[6:7]
	global_load_dwordx3 v[30:32], v[4:5], off
	global_load_dwordx3 v[26:28], v[4:5], off offset:512
	global_load_dwordx4 v[2:5], v177, s[20:21]
	global_load_dwordx4 v[6:9], v178, s[20:21]
	global_load_dwordx4 v[10:13], v179, s[20:21]
	global_load_dwordx4 v[14:17], v180, s[20:21]
	global_load_dwordx4 v[18:21], v181, s[20:21]
	global_load_dwordx4 v[22:25], v182, s[20:21]
	v_and_b32_e32 v38, 63, v0
	v_mov_b32_e32 v29, 0xff800000
	v_cmp_gt_u32_e64 s[0:1], 32, v38
	s_waitcnt lgkmcnt(0)
	s_cmpk_gt_i32 s26, 0x600
	s_cselect_b64 s[24:25], -1, 0
	s_cmpk_lt_i32 s26, 0x601
	s_cbranch_scc1 .LBB4_6
	s_and_saveexec_b64 s[8:9], s[14:15]
	s_cbranch_execz .LBB4_5
	v_or_b32_e32 v178, s29, v0
	v_mov_b32_e32 v179, 0
	v_lshl_add_u64 v[178:179], v[178:179], 4, s[6:7]
	global_load_dwordx4 v[178:181], v[178:179], off
	v_lshlrev_b32_e32 v177, 4, v0
	s_waitcnt vmcnt(0)
	ds_write_b128 v177, v[178:181] offset:2080

.LBB4_39:
	s_waitcnt vmcnt(5)
	v_rcp_f32_e32 v2, v133
	s_waitcnt vmcnt(4)
	v_rcp_f32_e32 v3, v132
	s_waitcnt vmcnt(3)
	v_rcp_f32_e32 v4, v131
	v_cmp_lt_f32_e32 vcc, 0, v133
	s_waitcnt vmcnt(2)
	v_rcp_f32_e32 v5, v130
	s_waitcnt vmcnt(1)
	v_rcp_f32_e32 v6, v129
	v_cndmask_b32_e32 v2, 0, v2, vcc
	v_cmp_lt_f32_e32 vcc, 0, v132
	s_waitcnt vmcnt(0)
	v_rcp_f32_e32 v7, v128
	s_getpc_b64 s[36:37]
	s_sub_u32 s36, s36, 0x9240
	s_subb_u32 s37, s37, 0
	v_lshlrev_b32_e32 v183, 6, v0
	v_min_u32_e32 v183, 0x1980, v183
	global_load_dword v183, v183, s[36:37]
	v_lshlrev_b32_e32 v182, 6, v38
	global_load_dword v182, v182, s[38:39]
	s_lshl_b32 s40, s29, 10
	s_add_u32 s40, s42, s40
	s_addc_u32 s41, s43, 0
	v_lshlrev_b32_e32 v181, 6, v0
	v_and_b32_e32 v181, 0x7fc0, v181
	global_load_dword v181, v181, s[40:41]
	s_mov_b32 s4, 0x42c80000
	v_cndmask_b32_e32 v3, 0, v3, vcc
	v_cmp_lt_f32_e32 vcc, 0, v131
	v_cmp_ngt_f32_e64 s[2:3], s4, v3
	s_mov_b64 s[6:7], 0
	v_cndmask_b32_e32 v4, 0, v4, vcc
	v_cmp_lt_f32_e32 vcc, 0, v130
	s_nop 1
	v_cndmask_b32_e32 v5, 0, v5, vcc
	v_cmp_lt_f32_e32 vcc, 0, v129
	s_nop 1
	v_cndmask_b32_e32 v6, 0, v6, vcc
	v_cmp_lt_f32_e32 vcc, 0, v128
	s_nop 1
	v_cndmask_b32_e32 v7, 0, v7, vcc
	v_cmp_ngt_f32_e32 vcc, s4, v2
	s_or_b64 s[2:3], vcc, s[2:3]
	v_cmp_ngt_f32_e32 vcc, s4, v4
	s_or_b64 s[2:3], s[2:3], vcc
	v_cmp_ngt_f32_e32 vcc, s4, v5
	s_or_b64 s[2:3], s[2:3], vcc
	v_cmp_ngt_f32_e32 vcc, s4, v6
	s_or_b64 s[2:3], s[2:3], vcc
	v_cmp_ngt_f32_e32 vcc, s4, v7
	s_or_b64 s[2:3], s[2:3], vcc
	v_cndmask_b32_e64 v8, 0, 1, s[2:3]
	v_cmp_ne_u32_e32 vcc, 0, v8
	s_cmp_eq_u64 vcc, 0
	s_cselect_b64 s[2:3], -1, 0
	v_cndmask_b32_e64 v8, 0, 1, s[2:3]
	s_nop 0
	v_readfirstlane_b32 s2, v8
	s_bitcmp0_b32 s2, 0
	s_cbranch_scc0 .LBB4_45
	s_cmp_lt_i32 s28, 4
	s_cbranch_scc1 .LBB4_46
	s_cmp_gt_i32 s28, 4
	s_cbranch_scc0 .LBB4_47
	s_mov_b64 s[4:5], -1
	v_mov_b32_e32 v8, 0
	s_cmp_gt_i32 s28, 5
	v_mov_b32_e32 v167, 0
	v_mov_b32_e32 v166, 0
	v_mov_b32_e32 v165, 0
	v_mov_b32_e32 v164, 0
	v_mov_b32_e32 v162, 0
	v_mov_b32_e32 v160, 0
	v_mov_b32_e32 v159, 0
	v_mov_b32_e32 v157, 0
	v_mov_b32_e32 v151, 0
	v_mov_b32_e32 v149, 0
	v_mov_b32_e32 v147, 0
	v_mov_b32_e32 v146, 0
	v_mov_b32_e32 v144, 0
	v_mov_b32_e32 v143, 0
	v_mov_b32_e32 v152, 0
	v_mov_b32_e32 v153, 0
	v_mov_b32_e32 v154, 0
	v_mov_b32_e32 v155, 0
	v_mov_b32_e32 v156, 0
	v_mov_b32_e32 v158, 0
	v_mov_b32_e32 v161, 0
	v_mov_b32_e32 v163, 0
	v_mov_b32_e32 v168, 0
	v_mov_b32_e32 v169, 0
	v_mov_b32_e32 v170, 0
	v_mov_b32_e32 v171, 0
	v_mov_b32_e32 v172, 0
	v_mov_b32_e32 v173, 0
	v_mov_b32_e32 v174, 0
	v_mov_b32_e32 v145, 0
	v_mov_b32_e32 v148, 0
	v_mov_b32_e32 v150, 0
	s_cbranch_scc0 .LBB4_50
	s_cmp_eq_u32 s28, 6
	s_cbranch_scc0 .LBB4_49
	v_mov_b32_e32 v145, 0
	v_mov_b32_e32 v148, 0
	v_mov_b32_e32 v150, 0
	v_mov_b32_e32 v143, 0
	v_mov_b32_e32 v144, 0
	v_mov_b32_e32 v146, 0
	v_mov_b32_e32 v147, 0
	v_mov_b32_e32 v149, 0
	v_mov_b32_e32 v151, 0
	v_mov_b32_e32 v152, 0
	v_mov_b32_e32 v153, 0
	v_mov_b32_e32 v154, 0
	v_mov_b32_e32 v155, 0
	v_mov_b32_e32 v156, 0
	v_mov_b32_e32 v158, 0
	v_mov_b32_e32 v161, 0
	v_mov_b32_e32 v163, 0
	v_mov_b32_e32 v157, 0
	v_mov_b32_e32 v159, 0
	v_mov_b32_e32 v160, 0
	v_mov_b32_e32 v162, 0
	v_mov_b32_e32 v164, 0
	v_mov_b32_e32 v165, 0
	v_mov_b32_e32 v166, 0
	v_mov_b32_e32 v167, 0
	v_mov_b32_e32 v168, 0
	v_mov_b32_e32 v169, 0
	v_mov_b32_e32 v170, 0
	v_mov_b32_e32 v171, 0
	v_mov_b32_e32 v172, 0
	v_mov_b32_e32 v173, 0
	v_mov_b32_e32 v174, 0
	v_fma_mix_f32 v148, v43, v7, v148 op_sel_hi:[1,0,0]
	v_fma_mix_f32 v150, v45, v7, v150 op_sel_hi:[1,0,0]
	v_fma_mix_f32 v143, v50, v7, v143 op_sel_hi:[1,0,0]
	v_fma_mix_f32 v144, v54, v7, v144 op_sel_hi:[1,0,0]
	v_fma_mix_f32 v146, v58, v7, v146 op_sel_hi:[1,0,0]
	v_fma_mix_f32 v147, v61, v7, v147 op_sel_hi:[1,0,0]
	v_fma_mix_f32 v149, v64, v7, v149 op_sel_hi:[1,0,0]
	v_fma_mix_f32 v151, v66, v7, v151 op_sel_hi:[1,0,0]
	v_fma_mix_f32 v152, v43, v7, v152 op_sel:[1,0,0] op_sel_hi:[1,0,0]
	v_fma_mix_f32 v153, v45, v7, v153 op_sel:[1,0,0] op_sel_hi:[1,0,0]
	v_fma_mix_f32 v154, v50, v7, v154 op_sel:[1,0,0] op_sel_hi:[1,0,0]
	v_fma_mix_f32 v155, v54, v7, v155 op_sel:[1,0,0] op_sel_hi:[1,0,0]
	v_fma_mix_f32 v156, v58, v7, v156 op_sel:[1,0,0] op_sel_hi:[1,0,0]
	v_fma_mix_f32 v158, v61, v7, v158 op_sel:[1,0,0] op_sel_hi:[1,0,0]
	v_fma_mix_f32 v161, v64, v7, v161 op_sel:[1,0,0] op_sel_hi:[1,0,0]
	v_fma_mix_f32 v163, v66, v7, v163 op_sel:[1,0,0] op_sel_hi:[1,0,0]
	v_fma_mix_f32 v157, v72, v7, v157 op_sel_hi:[1,0,0]
	v_fma_mix_f32 v159, v76, v7, v159 op_sel_hi:[1,0,0]
	v_fma_mix_f32 v160, v83, v7, v160 op_sel_hi:[1,0,0]
	v_fma_mix_f32 v162, v85, v7, v162 op_sel_hi:[1,0,0]
	v_fma_mix_f32 v164, v89, v7, v164 op_sel_hi:[1,0,0]
	v_fma_mix_f32 v165, v92, v7, v165 op_sel_hi:[1,0,0]
	v_fma_mix_f32 v166, v95, v7, v166 op_sel_hi:[1,0,0]
	v_fma_mix_f32 v167, v96, v7, v167 op_sel_hi:[1,0,0]
	v_fma_mix_f32 v168, v72, v7, v168 op_sel:[1,0,0] op_sel_hi:[1,0,0]
	v_fma_mix_f32 v169, v76, v7, v169 op_sel:[1,0,0] op_sel_hi:[1,0,0]
	v_fma_mix_f32 v170, v83, v7, v170 op_sel:[1,0,0] op_sel_hi:[1,0,0]
	v_fma_mix_f32 v171, v85, v7, v171 op_sel:[1,0,0] op_sel_hi:[1,0,0]
	v_fma_mix_f32 v172, v89, v7, v172 op_sel:[1,0,0] op_sel_hi:[1,0,0]
	v_fma_mix_f32 v173, v92, v7, v173 op_sel:[1,0,0] op_sel_hi:[1,0,0]
	v_fma_mix_f32 v174, v95, v7, v174 op_sel:[1,0,0] op_sel_hi:[1,0,0]
	v_fma_mix_f32 v145, v96, v7, v145 op_sel:[1,0,0] op_sel_hi:[1,0,0]
	s_branch .LBB4_50

amdhsa.kernels:
  - .agpr_count:     0
    .args:
      - .actual_access:  read_only
        .address_space:  global
        .offset:         0
        .size:           8
        .value_kind:     global_buffer
      - .actual_access:  read_only
        .address_space:  global
        .offset:         8
        .size:           8
        .value_kind:     global_buffer
      - .actual_access:  read_only
        .address_space:  global
        .offset:         16
        .size:           8
        .value_kind:     global_buffer
      - .actual_access:  read_only
        .address_space:  global
        .offset:         24
        .size:           8
        .value_kind:     global_buffer
      - .actual_access:  write_only
        .address_space:  global
        .offset:         32
        .size:           8
        .value_kind:     global_buffer
      - .actual_access:  write_only
        .address_space:  global
        .offset:         40
        .size:           8
        .value_kind:     global_buffer
      - .actual_access:  write_only
        .address_space:  global
        .offset:         48
        .size:           8
        .value_kind:     global_buffer
      - .actual_access:  write_only
        .address_space:  global
        .offset:         56
        .size:           8
        .value_kind:     global_buffer
      - .actual_access:  write_only
        .address_space:  global
        .offset:         64
        .size:           8
        .value_kind:     global_buffer
      - .actual_access:  write_only
        .address_space:  global
        .offset:         72
        .size:           8
        .value_kind:     global_buffer
      - .actual_access:  write_only
        .address_space:  global
        .offset:         80
        .size:           8
        .value_kind:     global_buffer
      - .actual_access:  write_only
        .address_space:  global
        .offset:         88
        .size:           8
        .value_kind:     global_buffer
      - .actual_access:  write_only
        .address_space:  global
        .offset:         96
        .size:           8
        .value_kind:     global_buffer
      - .actual_access:  write_only
        .address_space:  global
        .offset:         104
        .size:           8
        .value_kind:     global_buffer
      - .actual_access:  write_only
        .address_space:  global
        .offset:         112
        .size:           8
        .value_kind:     global_buffer
    .group_segment_fixed_size: 67584
    .kernarg_segment_align: 8
    .kernarg_segment_size: 120
    .language:       OpenCL C
    .language_version:
      - 2
      - 0
    .max_flat_workgroup_size: 1024
    .name:           _Z6k_sortPKfS0_PKiS2_PiP15HIP_vector_typeIfLj4EEPfS7_S3_S7_S7_S3_S3_S6_S6_
    .private_segment_fixed_size: 0
    .sgpr_count:     58
    .sgpr_spill_count: 0
    .symbol:         _Z6k_sortPKfS0_PKiS2_PiP15HIP_vector_typeIfLj4EEPfS7_S3_S7_S7_S3_S3_S6_S6_.kd
    .uniform_work_group_size: 1
    .uses_dynamic_stack: false
    .vgpr_count:     48
    .vgpr_spill_count: 0
    .wavefront_size: 64
  - .agpr_count:     0
    .args:
      - .actual_access:  read_only
        .address_space:  global
        .offset:         0
        .size:           8
        .value_kind:     global_buffer
      - .actual_access:  read_only
        .address_space:  global
        .offset:         8
        .size:           8
        .value_kind:     global_buffer
      - .actual_access:  read_only
        .address_space:  global
        .offset:         16
        .size:           8
        .value_kind:     global_buffer
      - .actual_access:  read_only
        .address_space:  global
        .offset:         24
        .size:           8
        .value_kind:     global_buffer
      - .actual_access:  read_only
        .address_space:  global
        .offset:         32
        .size:           8
        .value_kind:     global_buffer
      - .actual_access:  read_only
        .address_space:  global
        .offset:         40
        .size:           8
        .value_kind:     global_buffer
      - .actual_access:  read_only
        .address_space:  global
        .offset:         48
        .size:           8
        .value_kind:     global_buffer
      - .actual_access:  write_only
        .address_space:  global
        .offset:         56
        .size:           8
        .value_kind:     global_buffer
    .group_segment_fixed_size: 145952
    .kernarg_segment_align: 8
    .kernarg_segment_size: 64
    .language:       OpenCL C
    .language_version:
      - 2
      - 0
    .max_flat_workgroup_size: 512
    .name:           _Z7k_finalPK15HIP_vector_typeIfLj4EES2_PKiS4_PKfS6_PKDF16_Pf
    .private_segment_fixed_size: 0
    .sgpr_count:     34
    .sgpr_spill_count: 0
    .symbol:         _Z7k_finalPK15HIP_vector_typeIfLj4EES2_PKiS4_PKfS6_PKDF16_Pf.kd
    .uniform_work_group_size: 1
    .uses_dynamic_stack: false
    .vgpr_count:     177
    .vgpr_spill_count: 0
    .wavefront_size: 64
  - .agpr_count:     0
    .args:
      - .actual_access:  read_only
        .address_space:  global
        .offset:         0
        .size:           8
        .value_kind:     global_buffer
      - .actual_access:  read_only
        .address_space:  global
        .offset:         8
        .size:           8
        .value_kind:     global_buffer
      - .actual_access:  read_only
        .address_space:  global
        .offset:         16
        .size:           8
        .value_kind:     global_buffer
      - .actual_access:  read_only
        .address_space:  global
        .offset:         24
        .size:           8
        .value_kind:     global_buffer
      - .actual_access:  read_only
        .address_space:  global
        .offset:         32
        .size:           8
        .value_kind:     global_buffer
      - .actual_access:  read_only
        .address_space:  global
        .offset:         40
        .size:           8
        .value_kind:     global_buffer
      - .actual_access:  read_only
        .address_space:  global
        .offset:         48
        .size:           8
        .value_kind:     global_buffer
      - .actual_access:  read_only
        .address_space:  global
        .offset:         56
        .size:           8
        .value_kind:     global_buffer
      - .actual_access:  read_only
        .address_space:  global
        .offset:         64
        .size:           8
        .value_kind:     global_buffer
      - .address_space:  global
        .offset:         72
        .size:           8
        .value_kind:     global_buffer
      - .actual_access:  read_only
        .address_space:  global
        .offset:         80
        .size:           8
        .value_kind:     global_buffer
      - .actual_access:  read_only
        .address_space:  global
        .offset:         88
        .size:           8
        .value_kind:     global_buffer
      - .actual_access:  read_only
        .address_space:  global
        .offset:         96
        .size:           8
        .value_kind:     global_buffer
      - .actual_access:  write_only
        .address_space:  global
        .offset:         104
        .size:           8
        .value_kind:     global_buffer
      - .address_space:  global
        .offset:         112
        .size:           8
        .value_kind:     global_buffer
      - .actual_access:  write_only
        .address_space:  global
        .offset:         120
        .size:           8
        .value_kind:     global_buffer
      - .actual_access:  write_only
        .address_space:  global
        .offset:         128
        .size:           8
        .value_kind:     global_buffer
      - .actual_access:  write_only
        .address_space:  global
        .offset:         136
        .size:           8
        .value_kind:     global_buffer
      - .actual_access:  write_only
        .address_space:  global
        .offset:         144
        .size:           8
        .value_kind:     global_buffer
    .group_segment_fixed_size: 30384
    .kernarg_segment_align: 8
    .kernarg_segment_size: 152
    .language:       OpenCL C
    .language_version:
      - 2
      - 0
    .max_flat_workgroup_size: 512
    .name:           _Z6k_iterILb1ELb0EEvPKfS1_PKiPK15HIP_vector_typeIfLj4EES7_S1_S1_S3_S1_PfS8_S1_S3_PDF16_PS5_SA_PiSA_SB_
    .private_segment_fixed_size: 0
    .sgpr_count:     108
    .sgpr_spill_count: 0
    .symbol:         _Z6k_iterILb1ELb0EEvPKfS1_PKiPK15HIP_vector_typeIfLj4EES7_S1_S1_S3_S1_PfS8_S1_S3_PDF16_PS5_SA_PiSA_SB_.kd
    .uniform_work_group_size: 1
    .uses_dynamic_stack: false
    .vgpr_count:     256
    .vgpr_spill_count: 0
    .wavefront_size: 64
  - .agpr_count:     0
    .args:
      - .actual_access:  read_only
        .address_space:  global
        .offset:         0
        .size:           8
        .value_kind:     global_buffer
      - .actual_access:  read_only
        .address_space:  global
        .offset:         8
        .size:           8
        .value_kind:     global_buffer
      - .actual_access:  read_only
        .address_space:  global
        .offset:         16
        .size:           8
        .value_kind:     global_buffer
      - .actual_access:  read_only
        .address_space:  global
        .offset:         24
        .size:           8
        .value_kind:     global_buffer
      - .actual_access:  read_only
        .address_space:  global
        .offset:         32
        .size:           8
        .value_kind:     global_buffer
      - .actual_access:  read_only
        .address_space:  global
        .offset:         40
        .size:           8
        .value_kind:     global_buffer
      - .actual_access:  read_only
        .address_space:  global
        .offset:         48
        .size:           8
        .value_kind:     global_buffer
      - .actual_access:  read_only
        .address_space:  global
        .offset:         56
        .size:           8
        .value_kind:     global_buffer
      - .actual_access:  read_only
        .address_space:  global
        .offset:         64
        .size:           8
        .value_kind:     global_buffer
      - .address_space:  global
        .offset:         72
        .size:           8
        .value_kind:     global_buffer
      - .actual_access:  read_only
        .address_space:  global
        .offset:         80
        .size:           8
        .value_kind:     global_buffer
      - .actual_access:  read_only
        .address_space:  global
        .offset:         88
        .size:           8
        .value_kind:     global_buffer
      - .actual_access:  read_only
        .address_space:  global
        .offset:         96
        .size:           8
        .value_kind:     global_buffer
      - .actual_access:  read_only
        .address_space:  global
        .offset:         104
        .size:           8
        .value_kind:     global_buffer
      - .actual_access:  read_only
        .address_space:  global
        .offset:         112
        .size:           8
        .value_kind:     global_buffer
      - .actual_access:  read_only
        .address_space:  global
        .offset:         120
        .size:           8
        .value_kind:     global_buffer
      - .actual_access:  read_only
        .address_space:  global
        .offset:         128
        .size:           8
        .value_kind:     global_buffer
      - .actual_access:  read_only
        .address_space:  global
        .offset:         136
        .size:           8
        .value_kind:     global_buffer
      - .actual_access:  read_only
        .address_space:  global
        .offset:         144
        .size:           8
        .value_kind:     global_buffer
    .group_segment_fixed_size: 5808
    .kernarg_segment_align: 8
    .kernarg_segment_size: 152
    .language:       OpenCL C
    .language_version:
      - 2
      - 0
    .max_flat_workgroup_size: 512
    .name:           _Z6k_iterILb0ELb0EEvPKfS1_PKiPK15HIP_vector_typeIfLj4EES7_S1_S1_S3_S1_PfS8_S1_S3_PDF16_PS5_SA_PiSA_SB_
    .private_segment_fixed_size: 0
    .sgpr_count:     46
    .sgpr_spill_count: 0
    .symbol:         _Z6k_iterILb0ELb0EEvPKfS1_PKiPK15HIP_vector_typeIfLj4EES7_S1_S1_S3_S1_PfS8_S1_S3_PDF16_PS5_SA_PiSA_SB_.kd
    .uniform_work_group_size: 1
    .uses_dynamic_stack: false
    .vgpr_count:     184
    .vgpr_spill_count: 0
    .wavefront_size: 64
  - .agpr_count:     0
    .args:
      - .actual_access:  read_only
        .address_space:  global
        .offset:         0
        .size:           8
        .value_kind:     global_buffer
      - .actual_access:  read_only
        .address_space:  global
        .offset:         8
        .size:           8
        .value_kind:     global_buffer
      - .actual_access:  read_only
        .address_space:  global
        .offset:         16
        .size:           8
        .value_kind:     global_buffer
      - .actual_access:  read_only
        .address_space:  global
        .offset:         24
        .size:           8
        .value_kind:     global_buffer
      - .actual_access:  read_only
        .address_space:  global
        .offset:         32
        .size:           8
        .value_kind:     global_buffer
      - .actual_access:  read_only
        .address_space:  global
        .offset:         40
        .size:           8
        .value_kind:     global_buffer
      - .actual_access:  read_only
        .address_space:  global
        .offset:         48
        .size:           8
        .value_kind:     global_buffer
      - .actual_access:  read_only
        .address_space:  global
        .offset:         56
        .size:           8
        .value_kind:     global_buffer
      - .actual_access:  read_only
        .address_space:  global
        .offset:         64
        .size:           8
        .value_kind:     global_buffer
      - .address_space:  global
        .offset:         72
        .size:           8
        .value_kind:     global_buffer
      - .actual_access:  write_only
        .address_space:  global
        .offset:         80
        .size:           8
        .value_kind:     global_buffer
      - .actual_access:  read_only
        .address_space:  global
        .offset:         88
        .size:           8
        .value_kind:     global_buffer
      - .actual_access:  read_only
        .address_space:  global
        .offset:         96
        .size:           8
        .value_kind:     global_buffer
      - .actual_access:  read_only
        .address_space:  global
        .offset:         104
        .size:           8
        .value_kind:     global_buffer
      - .actual_access:  read_only
        .address_space:  global
        .offset:         112
        .size:           8
        .value_kind:     global_buffer
      - .actual_access:  read_only
        .address_space:  global
        .offset:         120
        .size:           8
        .value_kind:     global_buffer
      - .actual_access:  read_only
        .address_space:  global
        .offset:         128
        .size:           8
        .value_kind:     global_buffer
      - .actual_access:  read_only
        .address_space:  global
        .offset:         136
        .size:           8
        .value_kind:     global_buffer
      - .actual_access:  read_only
        .address_space:  global
        .offset:         144
        .size:           8
        .value_kind:     global_buffer
    .group_segment_fixed_size: 5808
    .kernarg_segment_align: 8
    .kernarg_segment_size: 152
    .language:       OpenCL C
    .language_version:
      - 2
      - 0
    .max_flat_workgroup_size: 512
    .name:           _Z6k_iterILb0ELb1EEvPKfS1_PKiPK15HIP_vector_typeIfLj4EES7_S1_S1_S3_S1_PfS8_S1_S3_PDF16_PS5_SA_PiSA_SB_
    .private_segment_fixed_size: 0
    .sgpr_count:     50
    .sgpr_spill_count: 0
    .symbol:         _Z6k_iterILb0ELb1EEvPKfS1_PKiPK15HIP_vector_typeIfLj4EES7_S1_S1_S3_S1_PfS8_S1_S3_PDF16_PS5_SA_PiSA_SB_.kd
    .uniform_work_group_size: 1
    .uses_dynamic_stack: false
    .vgpr_count:     184
    .vgpr_spill_count: 0
    .wavefront_size: 64
